# L0 attention: workgroups 0-15 (which carry the extra context-query items) no longer convert weights in the idle slot; their 1152 tiles go to the router-phase drain; plus static prio
# baseline (speedup 1.0000x reference)
.LBB0_643:
	s_not_b32 s0, s41
	s_add_i32 s42, s46, s0
	s_mov_b64 s[0:1], -1
	s_cmpk_gt_i32 s42, 0x87
	s_waitcnt vmcnt(0)
	v_lshlrev_b32_e32 v172, 2, v184
	s_cbranch_scc0 .LBB0_720
	s_cmp_lt_u32 s41, 16
	s_cbranch_scc1 .LBB0_719
	s_ashr_i32 s0, s47, 6
	s_add_i32 s1, s41, -16
	s_lshl_b32 s1, s1, 3
	s_add_i32 s40, s1, s0
	s_add_u32 s41, s6, 0x17458000
	s_mulk_i32 s0, 0x2400
	s_addc_u32 s43, s7, 0
	s_add_i32 s0, s0, 0
	s_add_u32 s44, s6, 0x7458000
	s_addc_u32 s45, s7, 0
	s_add_u32 s47, s6, 0x6458000
	s_addc_u32 s48, s7, 0
	s_add_u32 s49, s6, 0x5458000
	s_addc_u32 s50, s7, 0
	s_add_u32 s51, s6, 0x4d58000
	s_addc_u32 s52, s7, 0
	s_add_u32 s53, s6, 0x158000
	s_addc_u32 s54, s7, 0
	s_add_u32 s55, s6, 0x3390c000
	v_lshlrev_b32_e32 v2, 4, v184
	s_addc_u32 s56, s7, 0
	v_lshlrev_b32_e32 v0, 2, v184
	v_and_b32_e32 v78, 48, v2
	s_add_u32 s57, s6, 0x35e0c000
	v_lshlrev_b32_e32 v2, 1, v184
	v_and_b32_e32 v82, 48, v184
	v_and_b32_e32 v0, 60, v0
	v_bfe_u32 v83, v184, 2, 4
	s_addc_u32 s58, s7, 0
	v_and_b32_e32 v2, 0x60, v2
	v_and_b32_e32 v8, 7, v184
	v_bfe_u32 v87, v184, 3, 3
	v_mov_b32_e32 v77, 0
	v_add_u32_e32 v1, s0, v82
	v_mul_u32_u24_e32 v3, 0x50, v0
	v_add_u32_e32 v4, s0, v78
	v_mul_u32_u24_e32 v5, 0x50, v83
	s_add_u32 s59, s6, 0x3760c000
	v_add_u32_e32 v6, s0, v2
	v_mul_u32_u24_e32 v7, 0x90, v0
	v_lshlrev_b32_e32 v2, 3, v8
	v_lshl_add_u32 v8, v8, 4, s0
	v_mul_u32_u24_e32 v9, 0x90, v87
	s_mul_i32 s40, s40, 9
	s_mov_b32 s1, 0
	v_mov_b32_e32 v79, v77
	v_or_b32_e32 v84, 16, v83
	v_or_b32_e32 v85, 32, v83
	v_or_b32_e32 v86, 48, v83
	s_addc_u32 s60, s7, 0
	v_or_b32_e32 v88, 8, v87
	v_or_b32_e32 v89, 16, v87
	v_or_b32_e32 v90, 24, v87
	v_or_b32_e32 v91, 32, v87
	v_or_b32_e32 v92, 40, v87
	v_or_b32_e32 v93, 48, v87
	v_or_b32_e32 v94, 56, v87
	s_mov_b32 s65, -9
	s_add_i32 s61, 0, 0x204f8
	s_movk_i32 s62, 0x2000
	s_movk_i32 s63, 0x4000
	s_movk_i32 s64, 0x6000
	s_mov_b32 s66, 0x12000
	s_mov_b32 s67, 0xc3e00000
	v_add_u32_e32 v95, v1, v3
	v_add_u32_e32 v96, v4, v5
	s_movk_i32 s68, 0x3000
	s_movk_i32 s69, 0x5000
	s_movk_i32 s70, 0x7000
	s_add_i32 s71, 0, 0x204c0
	s_add_i32 s72, 0, 0x204b8
	s_add_i32 s73, 0, 0x204b0
	s_add_i32 s74, 0, 0x204a8
	s_add_i32 s75, 0, 0x20458
	s_add_i32 s76, 0, 0x20448
	s_add_i32 s77, 0, 0x20440
	s_mov_b32 s78, 0x9000
	s_mov_b32 s79, 0x1b000
	s_mov_b32 s80, 0x25000
	s_mov_b32 s81, 0x2e000
	s_mov_b32 s82, 0x37000
	s_mov_b32 s83, 0x41000
	s_mov_b32 s84, 0x4a000
	s_mov_b32 s85, 0x53000
	s_mov_b32 s86, 0x5d000
	s_mov_b32 s87, 0x66000
	s_mov_b32 s88, 0x6f000
	s_mov_b32 s89, 0x79000
	s_mov_b32 s90, 0x82000
	s_mov_b32 s91, 0x8b000
	v_add_u32_e32 v97, v6, v7
	v_lshlrev_b32_e32 v76, 1, v2
	v_lshlrev_b32_e32 v80, 2, v0
	v_mov_b32_e32 v98, 0x43e00000
	v_mov_b32_e32 v100, v77
	v_mov_b32_e32 v101, v77
	v_mov_b32_e32 v102, v77
	v_mov_b32_e32 v103, v77
	v_add_u32_e32 v99, v8, v9
	s_branch .LBB0_647

.LBB0_1058:
	s_add_i32 s1, s40, 0xffffff68
	s_lshl_b32 s0, s38, 3
	s_max_i32 s1, s1, 0
	s_mulk_i32 s1, 0x48
	s_add_i32 s0, s42, s0
	s_add_i32 s43, s0, s1
	s_cmpk_gt_i32 s43, 0x5fff
	s_mov_b32 s1, 0
	s_cbranch_scc1 .LBB0_1135
	s_lshl_b32 s44, s40, 3
	s_add_u32 s45, s10, 0x17458000
	s_mul_i32 s0, s42, 0x2400
	s_addc_u32 s46, s11, 0
	s_add_i32 s0, s0, 0
	s_add_u32 s47, s10, 0x7458000
	s_addc_u32 s48, s11, 0
	s_add_u32 s49, s10, 0x6458000
	s_addc_u32 s50, s11, 0
	s_add_u32 s51, s10, 0x5458000
	s_addc_u32 s52, s11, 0
	s_add_u32 s53, s10, 0x4d58000
	s_addc_u32 s54, s11, 0
	s_add_u32 s55, s10, 0x158000
	s_addc_u32 s56, s11, 0
	s_add_u32 s57, s10, 0x3390c000
	s_addc_u32 s58, s11, 0
	s_add_u32 s59, s10, 0x35e0c000
	v_lshlrev_b32_e32 v2, 1, v86
	v_and_b32_e32 v0, 60, v0
	v_and_b32_e32 v80, 48, v54
	s_addc_u32 s60, s11, 0
	v_and_b32_e32 v2, 0x60, v2
	v_and_b32_e32 v8, 7, v85
	v_lshrrev_b32_e32 v90, 3, v86
	v_mov_b32_e32 v79, 0
	v_add_u32_e32 v1, s0, v76
	v_mul_u32_u24_e32 v3, 0x50, v0
	v_add_u32_e32 v4, s0, v80
	v_mul_u32_u24_e32 v5, 0x50, v87
	s_add_u32 s61, s10, 0x3760c000
	v_add_u32_e32 v6, s0, v2
	v_mul_u32_u24_e32 v7, 0x90, v0
	v_lshlrev_b32_e32 v2, 3, v8
	v_lshl_add_u32 v8, v8, 4, s0
	v_mul_u32_u24_e32 v9, 0x90, v90
	v_mov_b32_e32 v81, v79
	v_or_b32_e32 v77, 16, v87
	v_or_b32_e32 v88, 32, v87
	v_or_b32_e32 v89, 48, v87
	s_addc_u32 s62, s11, 0
	v_or_b32_e32 v91, 8, v90
	v_or_b32_e32 v92, 16, v90
	v_or_b32_e32 v93, 24, v90
	v_or_b32_e32 v94, 32, v90
	v_or_b32_e32 v95, 40, v90
	v_or_b32_e32 v96, 48, v90
	v_or_b32_e32 v97, 56, v90
	s_add_i32 s63, 0, 0x204f8
	s_movk_i32 s64, 0x2000
	s_movk_i32 s65, 0x4000
	s_movk_i32 s66, 0x6000
	s_mov_b32 s67, 0x12000
	s_mov_b32 s68, 0xc3e00000
	v_add_u32_e32 v98, v1, v3
	v_add_u32_e32 v99, v4, v5
	s_movk_i32 s69, 0x3000
	s_movk_i32 s70, 0x5000
	s_movk_i32 s71, 0x7000
	s_add_i32 s72, 0, 0x204c0
	s_add_i32 s73, 0, 0x204b8
	s_add_i32 s74, 0, 0x204b0
	s_add_i32 s75, 0, 0x204a8
	s_add_i32 s76, 0, 0x20458
	s_add_i32 s77, 0, 0x20448
	s_add_i32 s78, 0, 0x20440
	s_mov_b32 s79, 0x9000
	s_mov_b32 s80, 0x1b000
	s_mov_b32 s81, 0x25000
	s_mov_b32 s82, 0x2e000
	s_mov_b32 s83, 0x37000
	s_mov_b32 s84, 0x41000
	s_mov_b32 s85, 0x4a000
	s_mov_b32 s86, 0x53000
	s_mov_b32 s87, 0x5d000
	s_mov_b32 s88, 0x66000
	s_mov_b32 s89, 0x6f000
	s_mov_b32 s90, 0x79000
	s_mov_b32 s91, 0x82000
	s_mov_b32 s92, 0x8b000
	v_add_u32_e32 v100, v6, v7
	v_lshlrev_b32_e32 v78, 1, v2
	v_lshlrev_b32_e32 v82, 2, v0
	v_mov_b32_e32 v101, 0x43e00000
	v_mov_b32_e32 v104, v79
	v_mov_b32_e32 v105, v79
	v_mov_b32_e32 v106, v79
	v_mov_b32_e32 v107, v79
	v_add_u32_e32 v102, v8, v9
	s_branch .LBB0_1062
